# baseline (speedup 1.0000x reference)
_Z13logits_kernelPKDv8_DF16bS1_PKfS3_PDv2_fS5_Pf:
	s_load_dwordx4 s[4:7], s[0:1], 0x0
	s_load_dwordx4 s[12:15], s[0:1], 0x10
	s_load_dwordx4 s[24:27], s[0:1], 0x20
	s_load_dwordx2 s[28:29], s[0:1], 0x30
	s_lshl_b32 s3, s2, 1
	s_and_b32 s3, s3, 14
	s_ashr_i32 s8, s2, 7
	s_bfe_u32 s10, s2, 0x40003
	s_add_i32 s3, s3, s8
	v_lshrrev_b32_e32 v1, 6, v0
	v_and_b32_e32 v2, 63, v0
	s_movk_i32 s11, 0x3000
	v_lshlrev_b32_e32 v2, 4, v2
	v_and_b32_e32 v5, 31, v0
	v_mad_u32_u24 v2, v1, s11, v2
	v_lshlrev_b32_e32 v5, 2, v5
	s_lshl_b32 s9, s3, 9
	v_add_u32_e32 v3, 0x1000, v2
	v_add_u32_e32 v4, 0x2000, v2
	v_add_u32_e32 v5, s9, v5
	s_mul_i32 s8, s10, 0xc000
	s_mul_i32 s9, s3, 0x30000
	s_waitcnt lgkmcnt(0)
	s_load_dword s22, s[14:15], 0x0
	global_load_dword v248, v5, s[12:13] nt
	global_load_dword v249, v5, s[12:13] offset:128 nt
	global_load_dword v250, v5, s[12:13] offset:256 nt
	global_load_dword v251, v5, s[12:13] offset:384 nt
	s_add_u32 s4, s4, s8
	s_addc_u32 s5, s5, 0
	s_add_u32 s6, s6, s9
	s_addc_u32 s7, s7, 0
	s_add_u32 s16, s6, 0xc000
	s_addc_u32 s17, s7, 0
	s_add_u32 s18, s6, 0x18000
	s_addc_u32 s19, s7, 0
	s_add_u32 s20, s6, 0x24000
	s_addc_u32 s21, s7, 0
	global_load_dwordx4 v[8:11], v2, s[4:5] nt
	global_load_dwordx4 v[56:59], v2, s[6:7] nt
	global_load_dwordx4 v[104:107], v2, s[16:17] nt
	global_load_dwordx4 v[152:155], v2, s[18:19] nt
	global_load_dwordx4 v[200:203], v2, s[20:21] nt
	global_load_dwordx4 v[12:15], v2, s[4:5] offset:1024 nt
	global_load_dwordx4 v[60:63], v2, s[6:7] offset:1024 nt
	global_load_dwordx4 v[108:111], v2, s[16:17] offset:1024 nt
	global_load_dwordx4 v[156:159], v2, s[18:19] offset:1024 nt
	global_load_dwordx4 v[204:207], v2, s[20:21] offset:1024 nt
	global_load_dwordx4 v[16:19], v2, s[4:5] offset:2048 nt
	global_load_dwordx4 v[64:67], v2, s[6:7] offset:2048 nt
	global_load_dwordx4 v[112:115], v2, s[16:17] offset:2048 nt
	global_load_dwordx4 v[160:163], v2, s[18:19] offset:2048 nt
	global_load_dwordx4 v[208:211], v2, s[20:21] offset:2048 nt
	global_load_dwordx4 v[20:23], v2, s[4:5] offset:3072 nt
	global_load_dwordx4 v[68:71], v2, s[6:7] offset:3072 nt
	global_load_dwordx4 v[116:119], v2, s[16:17] offset:3072 nt
	global_load_dwordx4 v[164:167], v2, s[18:19] offset:3072 nt
	global_load_dwordx4 v[212:215], v2, s[20:21] offset:3072 nt
	global_load_dwordx4 v[24:27], v3, s[4:5] nt
	global_load_dwordx4 v[72:75], v3, s[6:7] nt
	global_load_dwordx4 v[120:123], v3, s[16:17] nt
	global_load_dwordx4 v[168:171], v3, s[18:19] nt
	global_load_dwordx4 v[216:219], v3, s[20:21] nt
	global_load_dwordx4 v[28:31], v3, s[4:5] offset:1024 nt
	global_load_dwordx4 v[76:79], v3, s[6:7] offset:1024 nt
	global_load_dwordx4 v[124:127], v3, s[16:17] offset:1024 nt
	global_load_dwordx4 v[172:175], v3, s[18:19] offset:1024 nt
	global_load_dwordx4 v[220:223], v3, s[20:21] offset:1024 nt
	global_load_dwordx4 v[32:35], v3, s[4:5] offset:2048 nt
	global_load_dwordx4 v[80:83], v3, s[6:7] offset:2048 nt
	global_load_dwordx4 v[128:131], v3, s[16:17] offset:2048 nt
	global_load_dwordx4 v[176:179], v3, s[18:19] offset:2048 nt
	global_load_dwordx4 v[224:227], v3, s[20:21] offset:2048 nt
	global_load_dwordx4 v[36:39], v3, s[4:5] offset:3072 nt
	global_load_dwordx4 v[84:87], v3, s[6:7] offset:3072 nt
	global_load_dwordx4 v[132:135], v3, s[16:17] offset:3072 nt
	global_load_dwordx4 v[180:183], v3, s[18:19] offset:3072 nt
	global_load_dwordx4 v[228:231], v3, s[20:21] offset:3072 nt
	global_load_dwordx4 v[40:43], v4, s[4:5] nt
	global_load_dwordx4 v[88:91], v4, s[6:7] nt
	global_load_dwordx4 v[136:139], v4, s[16:17] nt
	global_load_dwordx4 v[184:187], v4, s[18:19] nt
	global_load_dwordx4 v[232:235], v4, s[20:21] nt
	global_load_dwordx4 v[44:47], v4, s[4:5] offset:1024 nt
	global_load_dwordx4 v[92:95], v4, s[6:7] offset:1024 nt
	global_load_dwordx4 v[140:143], v4, s[16:17] offset:1024 nt
	global_load_dwordx4 v[188:191], v4, s[18:19] offset:1024 nt
	global_load_dwordx4 v[236:239], v4, s[20:21] offset:1024 nt
	global_load_dwordx4 v[48:51], v4, s[4:5] offset:2048 nt
	global_load_dwordx4 v[96:99], v4, s[6:7] offset:2048 nt
	global_load_dwordx4 v[144:147], v4, s[16:17] offset:2048 nt
	global_load_dwordx4 v[192:195], v4, s[18:19] offset:2048 nt
	global_load_dwordx4 v[240:243], v4, s[20:21] offset:2048 nt
	global_load_dwordx4 v[52:55], v4, s[4:5] offset:3072 nt
	global_load_dwordx4 v[100:103], v4, s[6:7] offset:3072 nt
	global_load_dwordx4 v[148:151], v4, s[16:17] offset:3072 nt
	global_load_dwordx4 v[196:199], v4, s[18:19] offset:3072 nt
	global_load_dwordx4 v[244:247], v4, s[20:21] offset:3072 nt
	s_waitcnt vmcnt(58)
	v_mfma_f32_32x32x16_bf16 a[0:15], v[8:11], v[56:59], 0
	s_waitcnt vmcnt(57)
	v_mfma_f32_32x32x16_bf16 a[0:15], v[8:11], v[104:107], a[0:15]
	s_waitcnt vmcnt(56)
	v_mfma_f32_32x32x16_bf16 a[0:15], v[8:11], v[152:155], a[0:15]
	s_waitcnt vmcnt(55)
	v_mfma_f32_32x32x16_bf16 a[0:15], v[8:11], v[200:203], a[0:15]
	s_waitcnt vmcnt(53)
	v_mfma_f32_32x32x16_bf16 a[0:15], v[12:15], v[60:63], a[0:15]
	s_waitcnt vmcnt(52)
	v_mfma_f32_32x32x16_bf16 a[0:15], v[12:15], v[108:111], a[0:15]
	s_waitcnt vmcnt(51)
	v_mfma_f32_32x32x16_bf16 a[0:15], v[12:15], v[156:159], a[0:15]
	s_waitcnt vmcnt(50)
	v_mfma_f32_32x32x16_bf16 a[0:15], v[12:15], v[204:207], a[0:15]
	v_add_f32_e32 v8, 0, v248
	v_add_f32_e32 v8, v8, v249
	v_add_f32_e32 v8, v8, v250
	v_add_f32_e32 v8, v8, v251
	v_mov_b32_e32 v9, 0x3fb8aa3b
	s_waitcnt lgkmcnt(0)
	v_mul_f32_e32 v9, s22, v9
	v_exp_f32_e32 v9, v9
	v_add_f32_e32 v10, 0x2b8cbccc, v8
	v_div_scale_f32 v11, s[8:9], v10, v10, v9
	v_rcp_f32_e32 v12, v11
	v_div_scale_f32 v13, vcc, v9, v10, v9
	v_fma_f32 v14, -v11, v12, 1.0
	v_fmac_f32_e32 v12, v14, v12
	v_mul_f32_e32 v14, v13, v12
	v_fma_f32 v15, -v11, v14, v13
	v_fmac_f32_e32 v14, v15, v12
	v_fma_f32 v11, -v11, v14, v13
	v_div_fmas_f32 v11, v11, v12, v14
	v_div_fixup_f32 v9, v11, v10, v9
	v_lshlrev_b32_e32 v10, 2, v0
	v_add_u32_e32 v10, 0x4000, v10
	v_cmp_gt_u32_e32 vcc, 32, v0
	s_and_saveexec_b64 s[8:9], vcc
	ds_write2_b32 v10, v8, v9 offset0:128 offset1:160
	s_mov_b64 exec, s[8:9]
	s_waitcnt vmcnt(48)
	v_mfma_f32_32x32x16_bf16 a[0:15], v[16:19], v[64:67], a[0:15]
	s_waitcnt vmcnt(47)
	v_mfma_f32_32x32x16_bf16 a[0:15], v[16:19], v[112:115], a[0:15]
	s_waitcnt vmcnt(46)
	v_mfma_f32_32x32x16_bf16 a[0:15], v[16:19], v[160:163], a[0:15]
	s_waitcnt vmcnt(45)
	v_mfma_f32_32x32x16_bf16 a[0:15], v[16:19], v[208:211], a[0:15]
	s_waitcnt vmcnt(43)
	v_mfma_f32_32x32x16_bf16 a[0:15], v[20:23], v[68:71], a[0:15]
	s_waitcnt vmcnt(42)
	v_mfma_f32_32x32x16_bf16 a[0:15], v[20:23], v[116:119], a[0:15]
	s_waitcnt vmcnt(41)
	v_mfma_f32_32x32x16_bf16 a[0:15], v[20:23], v[164:167], a[0:15]
	s_waitcnt vmcnt(40)
	v_mfma_f32_32x32x16_bf16 a[0:15], v[20:23], v[212:215], a[0:15]
	s_waitcnt vmcnt(38)
	v_mfma_f32_32x32x16_bf16 a[0:15], v[24:27], v[72:75], a[0:15]
	s_waitcnt vmcnt(37)
	v_mfma_f32_32x32x16_bf16 a[0:15], v[24:27], v[120:123], a[0:15]
	s_waitcnt vmcnt(36)
	v_mfma_f32_32x32x16_bf16 a[0:15], v[24:27], v[168:171], a[0:15]
	s_waitcnt vmcnt(35)
	v_mfma_f32_32x32x16_bf16 a[0:15], v[24:27], v[216:219], a[0:15]
	s_waitcnt vmcnt(33)
	v_mfma_f32_32x32x16_bf16 a[0:15], v[28:31], v[76:79], a[0:15]
	s_waitcnt vmcnt(32)
	v_mfma_f32_32x32x16_bf16 a[0:15], v[28:31], v[124:127], a[0:15]
	s_waitcnt vmcnt(31)
	v_mfma_f32_32x32x16_bf16 a[0:15], v[28:31], v[172:175], a[0:15]
	s_waitcnt vmcnt(30)
	v_mfma_f32_32x32x16_bf16 a[0:15], v[28:31], v[220:223], a[0:15]
	s_waitcnt vmcnt(28)
	v_mfma_f32_32x32x16_bf16 a[0:15], v[32:35], v[80:83], a[0:15]
	s_waitcnt vmcnt(27)
	v_mfma_f32_32x32x16_bf16 a[0:15], v[32:35], v[128:131], a[0:15]
	s_waitcnt vmcnt(26)
	v_mfma_f32_32x32x16_bf16 a[0:15], v[32:35], v[176:179], a[0:15]
	s_waitcnt vmcnt(25)
	v_mfma_f32_32x32x16_bf16 a[0:15], v[32:35], v[224:227], a[0:15]
	s_waitcnt vmcnt(23)
	v_mfma_f32_32x32x16_bf16 a[0:15], v[36:39], v[84:87], a[0:15]
	s_waitcnt vmcnt(22)
	v_mfma_f32_32x32x16_bf16 a[0:15], v[36:39], v[132:135], a[0:15]
	s_waitcnt vmcnt(21)
	v_mfma_f32_32x32x16_bf16 a[0:15], v[36:39], v[180:183], a[0:15]
	s_waitcnt vmcnt(20)
	v_mfma_f32_32x32x16_bf16 a[0:15], v[36:39], v[228:231], a[0:15]
	s_waitcnt vmcnt(18)
	v_mfma_f32_32x32x16_bf16 a[0:15], v[40:43], v[88:91], a[0:15]
	s_waitcnt vmcnt(17)
	v_mfma_f32_32x32x16_bf16 a[0:15], v[40:43], v[136:139], a[0:15]
	s_waitcnt vmcnt(16)
	v_mfma_f32_32x32x16_bf16 a[0:15], v[40:43], v[184:187], a[0:15]
	s_waitcnt vmcnt(15)
	v_mfma_f32_32x32x16_bf16 a[0:15], v[40:43], v[232:235], a[0:15]
	s_waitcnt vmcnt(13)
	v_mfma_f32_32x32x16_bf16 a[0:15], v[44:47], v[92:95], a[0:15]
	s_waitcnt vmcnt(12)
	v_mfma_f32_32x32x16_bf16 a[0:15], v[44:47], v[140:143], a[0:15]
	s_waitcnt vmcnt(11)
	v_mfma_f32_32x32x16_bf16 a[0:15], v[44:47], v[188:191], a[0:15]
	s_waitcnt vmcnt(10)
	v_mfma_f32_32x32x16_bf16 a[0:15], v[44:47], v[236:239], a[0:15]
	s_waitcnt vmcnt(8)
	v_mfma_f32_32x32x16_bf16 a[0:15], v[48:51], v[96:99], a[0:15]
	s_waitcnt vmcnt(7)
	v_mfma_f32_32x32x16_bf16 a[0:15], v[48:51], v[144:147], a[0:15]
	s_waitcnt vmcnt(6)
	v_mfma_f32_32x32x16_bf16 a[0:15], v[48:51], v[192:195], a[0:15]
	s_waitcnt vmcnt(5)
	v_mfma_f32_32x32x16_bf16 a[0:15], v[48:51], v[240:243], a[0:15]
	v_mul_u32_u24_e32 v1, 0x1080, v1
	s_movk_i32 s4, 0x7f
	s_movk_i32 s6, 0x84
	v_cmp_lt_u32_e32 vcc, s4, v0
	v_lshrrev_b32_e32 v11, 3, v0
	v_and_b32_e32 v10, 31, v0
	v_and_b32_e32 v11, 4, v11
	v_mul_u32_u24_e32 v11, 0x84, v11
	v_lshlrev_b32_e32 v9, 2, v10
	v_bfe_u32 v6, v0, 2, 5
	v_and_b32_e32 v7, 3, v0
	v_add3_u32 v1, v1, v11, v9
	v_lshlrev_b32_e32 v8, 3, v7
	s_waitcnt vmcnt(3)
	v_mfma_f32_32x32x16_bf16 a[0:15], v[52:55], v[100:103], a[0:15]
	s_waitcnt vmcnt(2)
	v_mfma_f32_32x32x16_bf16 a[0:15], v[52:55], v[148:151], a[0:15]
	s_waitcnt vmcnt(1)
	v_mfma_f32_32x32x16_bf16 a[0:15], v[52:55], v[196:199], a[0:15]
	s_waitcnt vmcnt(0)
	v_mfma_f32_32x32x16_bf16 a[0:15], v[52:55], v[244:247], a[0:15]
	s_nop 11
	ds_write_b32 v1, a0
	ds_write_b32 v1, a1 offset:132
	ds_write_b32 v1, a2 offset:264
	ds_write_b32 v1, a3 offset:396
	ds_write_b32 v1, a4 offset:1056
	ds_write_b32 v1, a5 offset:1188
	ds_write_b32 v1, a6 offset:1320
	ds_write_b32 v1, a7 offset:1452
	ds_write_b32 v1, a8 offset:2112
	ds_write_b32 v1, a9 offset:2244
	ds_write_b32 v1, a10 offset:2376
	ds_write_b32 v1, a11 offset:2508
	ds_write_b32 v1, a12 offset:3168
	ds_write_b32 v1, a13 offset:3300
	ds_write_b32 v1, a14 offset:3432
	ds_write_b32 v1, a15 offset:3564
	v_bfe_u32 v6, v0, 2, 5
	v_and_b32_e32 v7, 3, v0
	v_lshlrev_b32_e32 v9, 3, v7
	v_readfirstlane_b32 s30, v0
	v_sub_u32_e32 v10, v6, v9
	s_waitcnt lgkmcnt(0)
	s_barrier
	s_cmpk_ge_u32 s30, 0x80
	s_cbranch_scc1 .Llg_k1
	v_mul_u32_u24_e32 v2, 0x84, v6
	v_lshlrev_b32_e32 v8, 5, v7
	v_add_u32_e32 v2, v2, v8
	v_add_u32_e32 v8, 0x4280, v8
	v_add_u32_e32 v3, 0x1080, v2
	v_add_u32_e32 v4, 0x2100, v2
	v_add_u32_e32 v5, 0x3180, v2
	ds_read_b128 v[48:51], v8
	ds_read_b128 v[52:55], v8 offset:16
	ds_read2_b32 v[16:17], v2 offset0:0 offset1:1
	ds_read2_b32 v[18:19], v2 offset0:2 offset1:3
	ds_read2_b32 v[20:21], v2 offset0:4 offset1:5
	ds_read2_b32 v[22:23], v2 offset0:6 offset1:7
	ds_read2_b32 v[24:25], v3 offset0:0 offset1:1
	ds_read2_b32 v[26:27], v3 offset0:2 offset1:3
	ds_read2_b32 v[28:29], v3 offset0:4 offset1:5
	ds_read2_b32 v[30:31], v3 offset0:6 offset1:7
	ds_read2_b32 v[32:33], v4 offset0:0 offset1:1
	ds_read2_b32 v[34:35], v4 offset0:2 offset1:3
	ds_read2_b32 v[36:37], v4 offset0:4 offset1:5
	ds_read2_b32 v[38:39], v4 offset0:6 offset1:7
	s_waitcnt lgkmcnt(4)
	ds_read2_b32 v[40:41], v5 offset0:0 offset1:1
	ds_read2_b32 v[42:43], v5 offset0:2 offset1:3
	ds_read2_b32 v[44:45], v5 offset0:4 offset1:5
	ds_read2_b32 v[46:47], v5 offset0:6 offset1:7
	s_waitcnt lgkmcnt(0)
	s_branch .Llg_join
